# v15 + scan: DMA addresses precomputed before the second step barrier, lean branch ladder at the step top; GLA pre image-store reads hoisted
# speedup vs baseline: 1.0052x; 1.0024x over previous
.LBB0_410:
	s_or_b64 exec, exec, s[2:3]
	v_add_u32_e32 v5, s17, v55
	v_add3_u32 v21, v5, v56, v54
	v_add_u32_e32 v160, 0xe000, v21
	ds_read_u16 v128, v21 offset:57344
	ds_read_u16 v129, v21 offset:57600
	ds_read_u16 v130, v160 offset:16384
	ds_read_u16 v131, v160 offset:16640
	ds_read_u16 v132, v21 offset:57856
	ds_read_u16 v133, v21 offset:58112
	ds_read_u16 v134, v160 offset:16896
	ds_read_u16 v135, v160 offset:17152
	ds_read_u16 v136, v21 offset:61440
	ds_read_u16 v137, v21 offset:61696
	ds_read_u16 v138, v160 offset:20480
	ds_read_u16 v139, v160 offset:20736
	ds_read_u16 v140, v21 offset:61952
	ds_read_u16 v141, v21 offset:62208
	ds_read_u16 v142, v160 offset:20992
	ds_read_u16 v143, v160 offset:21248
	ds_read_u16 v144, v160 offset:8192
	ds_read_u16 v145, v160 offset:8448
	ds_read_u16 v146, v160 offset:24576
	ds_read_u16 v147, v160 offset:24832
	ds_read_u16 v148, v160 offset:8704
	ds_read_u16 v149, v160 offset:8960
	ds_read_u16 v150, v160 offset:25088
	ds_read_u16 v151, v160 offset:25344
	ds_read_u16 v152, v160 offset:12288
	ds_read_u16 v153, v160 offset:12544
	ds_read_u16 v154, v160 offset:28672
	ds_read_u16 v155, v160 offset:28928
	ds_read_u16 v156, v160 offset:12800
	ds_read_u16 v157, v160 offset:13056
	ds_read_u16 v158, v160 offset:29184
	ds_read_u16 v159, v160 offset:29440
	s_and_b32 s2, s95, 3
	s_mul_i32 s2, s2, 17
	s_ashr_i32 s3, s95, 8
	v_exp_f32_e32 v28, v44
	v_exp_f32_e32 v29, v45
	s_add_i32 s2, s2, s3
	s_mulk_i32 s96, 0x44
	s_add_i32 s16, s2, s96
	s_waitcnt lgkmcnt(15)
	v_lshlrev_b32_e32 v33, 16, v129
	v_lshlrev_b32_e32 v32, 16, v128
	s_mov_b32 s2, 0x3db504f3
	v_pk_mul_f32 v[32:33], v[32:33], s[2:3] op_sel_hi:[1,0]
	v_exp_f32_e32 v20, v30
	v_add_u32_e32 v5, 0xe000, v21
	v_rcp_f32_e32 v30, v28
	v_rcp_f32_e32 v31, v29
	v_pk_mul_f32 v[28:29], v[28:29], v[32:33]
	v_exp_f32_e32 v26, v26
	v_cvt_pk_bf16_f32 v36, v28, v29
	v_exp_f32_e32 v27, v27
	v_exp_f32_e32 v24, v24
	v_exp_f32_e32 v25, v25
	s_waitcnt lgkmcnt(15)
	v_lshlrev_b32_e32 v28, 16, v130
	v_lshlrev_b32_e32 v29, 16, v131
	v_pk_mul_f32 v[32:33], v[30:31], v[28:29]
	v_pk_mul_f32 v[30:31], v[20:21], v[30:31] op_sel_hi:[0,1]
	v_cvt_pk_bf16_f32 v32, v32, v33
	v_add_u32_e32 v33, v57, v60
	ds_write_b16 v33, v36
	ds_write_b16_d16_hi v70, v36
	ds_write_b16 v33, v32 offset:16384
	ds_write_b16_d16_hi v70, v32 offset:16384
	v_pk_mul_f32 v[28:29], v[30:31], v[28:29]
	v_exp_f32_e32 v30, v34
	v_cvt_pk_bf16_f32 v28, v28, v29
	v_exp_f32_e32 v31, v35
	v_rcp_f32_e32 v32, v30
	v_exp_f32_e32 v22, v22
	v_exp_f32_e32 v23, v23
	s_waitcnt lgkmcnt(15)
	v_lshlrev_b32_e32 v35, 16, v133
	v_lshlrev_b32_e32 v34, 16, v132
	v_pk_mul_f32 v[34:35], v[34:35], s[2:3] op_sel_hi:[1,0]
	v_rcp_f32_e32 v33, v31
	v_pk_mul_f32 v[30:31], v[30:31], v[34:35]
	v_exp_f32_e32 v18, v18
	v_cvt_pk_bf16_f32 v29, v30, v31
	v_exp_f32_e32 v19, v19
	v_exp_f32_e32 v16, v16
	v_exp_f32_e32 v17, v17
	s_waitcnt lgkmcnt(15)
	v_lshlrev_b32_e32 v30, 16, v134
	v_lshlrev_b32_e32 v31, 16, v135
	v_pk_mul_f32 v[34:35], v[32:33], v[30:31]
	v_pk_mul_f32 v[32:33], v[20:21], v[32:33] op_sel_hi:[0,1]
	v_pk_mul_f32 v[30:31], v[32:33], v[30:31]
	v_cvt_pk_bf16_f32 v34, v34, v35
	ds_write_b16 v71, v29
	ds_write_b16_d16_hi v72, v29
	ds_write_b16 v71, v34 offset:16384
	ds_write_b16_d16_hi v72, v34 offset:16384
	v_cvt_pk_bf16_f32 v29, v30, v31
	ds_write_b64 v73, v[28:29] offset:32768
	v_rcp_f32_e32 v28, v26
	v_rcp_f32_e32 v29, v27
	v_exp_f32_e32 v6, v6
	s_waitcnt lgkmcnt(15)
	v_lshlrev_b32_e32 v30, 16, v136
	v_lshlrev_b32_e32 v31, 16, v137
	v_pk_mul_f32 v[30:31], v[30:31], s[2:3] op_sel_hi:[1,0]
	v_exp_f32_e32 v7, v7
	v_pk_mul_f32 v[26:27], v[26:27], v[30:31]
	s_ashr_i32 s17, s16, 31
	v_cvt_pk_bf16_f32 v32, v26, v27
	s_movk_i32 s10, 0x2000
	s_waitcnt lgkmcnt(15)
	v_lshlrev_b32_e32 v26, 16, v138
	v_lshlrev_b32_e32 v27, 16, v139
	v_pk_mul_f32 v[30:31], v[28:29], v[26:27]
	v_pk_mul_f32 v[28:29], v[20:21], v[28:29] op_sel_hi:[0,1]
	v_cvt_pk_bf16_f32 v30, v30, v31
	ds_write_b16 v74, v32
	ds_write_b16_d16_hi v75, v32
	ds_write_b16 v74, v30 offset:16384
	ds_write_b16_d16_hi v75, v30 offset:16384
	v_pk_mul_f32 v[26:27], v[28:29], v[26:27]
	v_rcp_f32_e32 v28, v24
	v_cvt_pk_bf16_f32 v26, v26, v27
	v_rcp_f32_e32 v29, v25
	s_waitcnt lgkmcnt(15)
	v_lshlrev_b32_e32 v30, 16, v140
	v_lshlrev_b32_e32 v31, 16, v141
	v_pk_mul_f32 v[30:31], v[30:31], s[2:3] op_sel_hi:[1,0]
	s_nop 0
	v_pk_mul_f32 v[24:25], v[24:25], v[30:31]
	s_nop 0
	v_cvt_pk_bf16_f32 v21, v24, v25
	s_waitcnt lgkmcnt(15)
	v_lshlrev_b32_e32 v24, 16, v142
	v_lshlrev_b32_e32 v25, 16, v143
	v_pk_mul_f32 v[30:31], v[28:29], v[24:25]
	v_pk_mul_f32 v[28:29], v[20:21], v[28:29] op_sel_hi:[0,1]
	v_cvt_pk_bf16_f32 v27, v30, v31
	v_pk_mul_f32 v[24:25], v[28:29], v[24:25]
	ds_write_b16 v76, v21
	ds_write_b16_d16_hi v77, v21
	ds_write_b16 v76, v27 offset:16384
	ds_write_b16_d16_hi v77, v27 offset:16384
	v_cvt_pk_bf16_f32 v27, v24, v25
	ds_write_b64 v78, v[26:27] offset:32768
	v_rcp_f32_e32 v24, v22
	v_rcp_f32_e32 v25, v23
	s_waitcnt lgkmcnt(15)
	v_lshlrev_b32_e32 v27, 16, v145
	v_lshlrev_b32_e32 v26, 16, v144
	v_pk_mul_f32 v[26:27], v[26:27], s[2:3] op_sel_hi:[1,0]
	s_nop 0
	v_pk_mul_f32 v[22:23], v[22:23], v[26:27]
	s_nop 0
	v_cvt_pk_bf16_f32 v21, v22, v23
	s_waitcnt lgkmcnt(15)
	v_lshlrev_b32_e32 v22, 16, v146
	v_lshlrev_b32_e32 v23, 16, v147
	v_pk_mul_f32 v[26:27], v[24:25], v[22:23]
	v_pk_mul_f32 v[24:25], v[20:21], v[24:25] op_sel_hi:[0,1]
	v_cvt_pk_bf16_f32 v26, v26, v27
	ds_write_b16 v79, v21
	ds_write_b16_d16_hi v80, v21
	ds_write_b16 v79, v26 offset:16384
	ds_write_b16_d16_hi v80, v26 offset:16384
	v_pk_mul_f32 v[22:23], v[24:25], v[22:23]
	v_rcp_f32_e32 v24, v18
	v_cvt_pk_bf16_f32 v22, v22, v23
	v_rcp_f32_e32 v25, v19
	s_waitcnt lgkmcnt(15)
	v_lshlrev_b32_e32 v26, 16, v148
	v_lshlrev_b32_e32 v27, 16, v149
	v_pk_mul_f32 v[26:27], v[26:27], s[2:3] op_sel_hi:[1,0]
	s_nop 0
	v_pk_mul_f32 v[18:19], v[18:19], v[26:27]
	s_nop 0
	v_cvt_pk_bf16_f32 v21, v18, v19
	s_waitcnt lgkmcnt(15)
	v_lshlrev_b32_e32 v18, 16, v150
	v_lshlrev_b32_e32 v19, 16, v151
	v_pk_mul_f32 v[26:27], v[24:25], v[18:19]
	v_pk_mul_f32 v[24:25], v[20:21], v[24:25] op_sel_hi:[0,1]
	v_cvt_pk_bf16_f32 v23, v26, v27
	v_pk_mul_f32 v[18:19], v[24:25], v[18:19]
	ds_write_b16 v81, v21
	ds_write_b16_d16_hi v82, v21
	ds_write_b16 v81, v23 offset:16384
	ds_write_b16_d16_hi v82, v23 offset:16384
	v_cvt_pk_bf16_f32 v23, v18, v19
	ds_write_b64 v83, v[22:23] offset:32768
	v_rcp_f32_e32 v18, v16
	v_rcp_f32_e32 v19, v17
	s_waitcnt lgkmcnt(15)
	v_lshlrev_b32_e32 v23, 16, v153
	v_lshlrev_b32_e32 v22, 16, v152
	v_pk_mul_f32 v[22:23], v[22:23], s[2:3] op_sel_hi:[1,0]
	s_nop 0
	v_pk_mul_f32 v[16:17], v[16:17], v[22:23]
	s_nop 0
	v_cvt_pk_bf16_f32 v21, v16, v17
	s_waitcnt lgkmcnt(15)
	v_lshlrev_b32_e32 v16, 16, v154
	v_lshlrev_b32_e32 v17, 16, v155
	v_pk_mul_f32 v[22:23], v[18:19], v[16:17]
	v_pk_mul_f32 v[18:19], v[20:21], v[18:19] op_sel_hi:[0,1]
	v_cvt_pk_bf16_f32 v22, v22, v23
	ds_write_b16 v84, v21
	ds_write_b16_d16_hi v85, v21
	ds_write_b16 v84, v22 offset:16384
	ds_write_b16_d16_hi v85, v22 offset:16384
	v_pk_mul_f32 v[16:17], v[18:19], v[16:17]
	v_rcp_f32_e32 v18, v6
	v_cvt_pk_bf16_f32 v16, v16, v17
	v_rcp_f32_e32 v19, v7
	s_waitcnt lgkmcnt(15)
	v_lshlrev_b32_e32 v22, 16, v156
	v_lshlrev_b32_e32 v23, 16, v157
	v_pk_mul_f32 v[22:23], v[22:23], s[2:3] op_sel_hi:[1,0]
	s_lshl_b64 s[2:3], s[16:17], 14
	v_pk_mul_f32 v[6:7], v[6:7], v[22:23]
	s_nop 0
	v_cvt_pk_bf16_f32 v17, v6, v7
	s_waitcnt lgkmcnt(15)
	v_lshlrev_b32_e32 v6, 16, v158
	v_lshlrev_b32_e32 v7, 16, v159
	v_pk_mul_f32 v[22:23], v[18:19], v[6:7]
	v_pk_mul_f32 v[18:19], v[20:21], v[18:19] op_sel_hi:[0,1]
	v_cvt_pk_bf16_f32 v5, v22, v23
	v_pk_mul_f32 v[6:7], v[18:19], v[6:7]
	ds_write_b16 v86, v17
	ds_write_b16_d16_hi v87, v17
	ds_write_b16 v86, v5 offset:16384
	ds_write_b16_d16_hi v87, v5 offset:16384
	v_cvt_pk_bf16_f32 v17, v6, v7
	v_add_u32_e32 v5, v58, v61
	ds_write_b64 v88, v[16:17] offset:32768
	s_waitcnt lgkmcnt(0)
	s_barrier
	ds_read_b128 v[16:19], v5
	v_add_u32_e32 v5, s81, v62
	ds_read_b128 v[20:23], v5 offset:16384
	v_add_u32_e32 v5, s82, v62
	ds_read_b128 v[24:27], v5 offset:16384
	v_add_u32_e32 v5, v58, v63
	s_waitcnt lgkmcnt(0)
	v_mfma_f32_16x16x32_bf16 v[20:23], v[20:23], v[16:19], 0
	v_cndmask_b32_e64 v6, 0, 1, s[26:27]
	v_cndmask_b32_e64 v7, 0, 1, s[18:19]
	v_mfma_f32_16x16x32_bf16 v[16:19], v[24:27], v[16:19], 0
	ds_read_b128 v[24:27], v5
	v_add_u32_e32 v5, s81, v65
	ds_read_b128 v[28:31], v5 offset:16384
	v_add_u32_e32 v5, s82, v65
	s_waitcnt lgkmcnt(0)
	v_mfma_f32_16x16x32_bf16 v[20:23], v[28:31], v[24:27], v[20:23]
	ds_read_b128 v[28:31], v5 offset:16384
	v_add_u32_e32 v5, v58, v66
	s_waitcnt lgkmcnt(0)
	v_mfma_f32_16x16x32_bf16 v[16:19], v[28:31], v[24:27], v[16:19]
	ds_read_b128 v[24:27], v5
	v_add_u32_e32 v5, s81, v67
	ds_read_b128 v[28:31], v5 offset:16384
	v_add_u32_e32 v5, s82, v67
	s_waitcnt lgkmcnt(0)
	v_mfma_f32_16x16x32_bf16 v[20:23], v[28:31], v[24:27], v[20:23]
	ds_read_b128 v[28:31], v5 offset:16384
	v_add_u32_e32 v5, v58, v68
	s_waitcnt lgkmcnt(0)
	v_mfma_f32_16x16x32_bf16 v[16:19], v[28:31], v[24:27], v[16:19]
	ds_read_b128 v[24:27], v5
	v_add_u32_e32 v5, s81, v69
	ds_read_b128 v[28:31], v5 offset:16384
	v_add_u32_e32 v5, s82, v69
	s_waitcnt lgkmcnt(0)
	v_mfma_f32_16x16x32_bf16 v[20:23], v[28:31], v[24:27], v[20:23]
	ds_read_b128 v[28:31], v5 offset:16384
	v_cndmask_b32_e64 v5, 0, 1, s[74:75]
	v_cndmask_b32_e64 v5, v6, v5, s[72:73]
	v_cndmask_b32_e64 v6, 0, 1, s[20:21]
	v_and_b32_e32 v5, 1, v5
	v_cndmask_b32_e64 v6, v7, v6, s[72:73]
	v_cmp_eq_u32_e32 vcc, 1, v5
	v_and_b32_e32 v6, 1, v6
	v_cndmask_b32_e64 v7, 0, 1, s[24:25]
	v_cndmask_b32_e32 v5, 0, v20, vcc
	v_cmp_eq_u32_e32 vcc, 1, v6
	v_cndmask_b32_e64 v20, 0, 1, s[22:23]
	v_cndmask_b32_e64 v7, v20, v7, s[72:73]
	v_cndmask_b32_e32 v6, 0, v21, vcc
	v_cndmask_b32_e64 v20, 0, 1, s[54:55]
	v_cndmask_b32_e64 v21, 0, 1, s[52:53]
	v_and_b32_e32 v7, 1, v7
	v_cndmask_b32_e64 v20, v21, v20, s[72:73]
	v_cmp_eq_u32_e32 vcc, 1, v7
	v_and_b32_e32 v20, 1, v20
	v_cvt_pk_bf16_f32 v6, v5, v6
	v_cndmask_b32_e32 v7, 0, v22, vcc
	v_cmp_eq_u32_e32 vcc, 1, v20
	s_waitcnt lgkmcnt(0)
	v_mfma_f32_16x16x32_bf16 v[16:19], v[28:31], v[24:27], v[16:19]
	v_cndmask_b32_e64 v5, 0, 1, s[58:59]
	v_cndmask_b32_e32 v20, 0, v23, vcc
	v_cvt_pk_bf16_f32 v7, v7, v20
	ds_write_b64 v89, v[6:7] offset:49152
	v_cndmask_b32_e64 v6, 0, 1, s[56:57]
	v_cndmask_b32_e64 v5, v6, v5, s[72:73]
	v_cndmask_b32_e64 v6, 0, 1, s[62:63]
	v_cndmask_b32_e64 v7, 0, 1, s[60:61]
	v_and_b32_e32 v5, 1, v5
	v_cndmask_b32_e64 v6, v7, v6, s[72:73]
	v_cmp_eq_u32_e32 vcc, 1, v5
	v_and_b32_e32 v6, 1, v6
	v_cndmask_b32_e64 v7, 0, 1, s[66:67]
	v_cndmask_b32_e32 v5, 0, v16, vcc
	v_cmp_eq_u32_e32 vcc, 1, v6
	v_cndmask_b32_e64 v16, 0, 1, s[64:65]
	v_cndmask_b32_e64 v7, v16, v7, s[72:73]
	v_cndmask_b32_e32 v6, 0, v17, vcc
	v_cndmask_b32_e64 v16, 0, 1, s[70:71]
	v_cndmask_b32_e64 v17, 0, 1, s[68:69]
	v_and_b32_e32 v7, 1, v7
	v_cndmask_b32_e64 v16, v17, v16, s[72:73]
	v_cmp_eq_u32_e32 vcc, 1, v7
	v_and_b32_e32 v16, 1, v16
	v_cvt_pk_bf16_f32 v6, v5, v6
	v_cndmask_b32_e32 v7, 0, v18, vcc
	v_cmp_eq_u32_e32 vcc, 1, v16
	v_add_u32_e32 v5, 0, v59
	s_add_u32 s72, s86, s2
	v_cndmask_b32_e32 v16, 0, v19, vcc
	v_cvt_pk_bf16_f32 v7, v7, v16
	ds_write_b64 v90, v[6:7] offset:49152
	s_waitcnt lgkmcnt(0)
	s_barrier
	ds_read_b128 v[128:131], v5
	ds_read_b128 v[132:135], v91
	ds_read_b128 v[136:139], v5 offset:32768
	ds_read_b128 v[140:143], v91 offset:32768
	ds_read_b128 v[144:147], v5 offset:49152
	s_addc_u32 s73, s87, s3
	v_lshlrev_b64 v[6:7], 4, v[12:13]
	v_lshl_add_u64 v[20:21], s[72:73], 0, v[6:7]
	s_add_u32 s96, s88, s2
	s_waitcnt lgkmcnt(4)
	global_store_dwordx4 v[20:21], v[128:131], off
	v_add_co_u32_e32 v20, vcc, s10, v20
	s_addc_u32 s97, s89, s3
	s_nop 0
	v_addc_co_u32_e32 v21, vcc, 0, v21, vcc
	s_waitcnt lgkmcnt(3)
	global_store_dwordx4 v[20:21], v[132:135], off
	v_lshl_add_u64 v[20:21], s[96:97], 0, v[6:7]
	s_lshl_b64 s[2:3], s[16:17], 13
	s_add_u32 s2, s90, s2
	s_addc_u32 s3, s91, s3
	s_waitcnt lgkmcnt(2)
	global_store_dwordx4 v[20:21], v[136:139], off
	v_add_co_u32_e32 v20, vcc, 0x2000, v20
	v_lshl_add_u64 v[6:7], s[2:3], 0, v[6:7]
	s_nop 0
	v_addc_co_u32_e32 v21, vcc, 0, v21, vcc
	s_waitcnt lgkmcnt(1)
	global_store_dwordx4 v[20:21], v[140:143], off
	s_waitcnt lgkmcnt(0)
	global_store_dwordx4 v[6:7], v[144:147], off
	s_and_saveexec_b64 s[2:3], s[76:77]
	s_cbranch_execz .LBB0_393
	v_add_u32_e32 v5, 0x22000, v5
	ds_read_b128 v[16:19], v5
	s_lshl_b64 s[16:17], s[16:17], 9
	s_add_u32 s16, s92, s16
	s_addc_u32 s17, s93, s17
	v_lshl_add_u64 v[6:7], v[12:13], 4, s[16:17]
	s_waitcnt lgkmcnt(0)
	global_store_dwordx4 v[6:7], v[16:19], off
	s_branch .LBB0_393

.LBB0_473:
	s_add_i32 s63, s62, -2
	s_add_i32 s9, s62, -6
	s_add_i32 s16, s61, 2
	s_sub_i32 s17, s61, 62
	s_and_b64 s[14:15], s[12:13], exec
	s_cselect_b32 s9, s9, s16
	s_cselect_b32 s17, s63, s17
	s_lshl_b32 s9, s9, 6
	s_lshl_b32 s17, s17, 6
	s_bitset1_b32 s17, 12
	s_cmp_gt_u32 s63, 3
	s_cselect_b32 s9, s9, s17
	s_cmp_lt_u32 s63, 2
	s_cbranch_scc1 .Lscan_w_first
	s_cmpk_eq_i32 s63, 0x43
	s_cbranch_scc1 .Lscan_w_last
	s_and_b64 vcc, exec, s[2:3]
	s_cbranch_vccz .Lscan_w_w0
	s_waitcnt vmcnt(8)
	s_branch .LBB0_482
.Lscan_w_w0:
	s_waitcnt vmcnt(9)
	s_branch .LBB0_482
.Lscan_w_last:
	s_waitcnt vmcnt(2)
	s_branch .LBB0_482
.Lscan_w_first:
	s_cmp_eq_u32 s63, 0
	s_cbranch_scc1 .Lscan_w_zero
	s_and_b64 vcc, exec, s[2:3]
	s_cbranch_vccz .Lscan_w1_w0
	s_waitcnt vmcnt(7)
	s_branch .LBB0_482
.Lscan_w1_w0:
	s_waitcnt vmcnt(8)
	s_branch .LBB0_482

.LBB0_482:
	s_bitcmp1_b32 s63, 0
	s_cselect_b64 s[14:15], -1, 0
	s_and_b64 s[16:17], s[14:15], exec
	s_cselect_b32 s16, 0xc400, 0
	s_add_i32 s16, s16, 0
	v_add_u32_e32 v16, s16, v132
	v_add_u32_e32 v17, s16, v136
	v_add_u32_e32 v18, s16, v137
	v_add3_u32 v16, v16, v133, v134
	v_add_u32_e32 v19, v17, v141
	v_add_u32_e32 v20, v18, v142
	s_barrier
	ds_read_b128 v[56:59], v19 offset:32768
	ds_read_b128 v[24:27], v20 offset:16384
	v_add_u32_e32 v20, v16, v140
	v_add_u32_e32 v21, v16, v143
	v_add_u32_e32 v22, v16, v144
	v_add_u32_e32 v23, v16, v145
	v_add_u32_e32 v16, v17, v146
	v_add_u32_e32 v17, v18, v147
	ds_read_b128 v[60:63], v16 offset:32768
	ds_read_b128 v[16:19], v17 offset:16384
	ds_read_b64_tr_b16 v[52:53], v20 offset:40960
	ds_read_b64_tr_b16 v[54:55], v20 offset:41472
	ds_read_b64_tr_b16 v[36:37], v20 offset:45056
	ds_read_b64_tr_b16 v[38:39], v20 offset:45568
	ds_read_b64_tr_b16 v[48:49], v21 offset:40960
	ds_read_b64_tr_b16 v[50:51], v21 offset:41472
	ds_read_b64_tr_b16 v[32:33], v21 offset:45056
	ds_read_b64_tr_b16 v[34:35], v21 offset:45568
	ds_read_b64_tr_b16 v[44:45], v22 offset:40960
	ds_read_b64_tr_b16 v[46:47], v22 offset:41472
	ds_read_b64_tr_b16 v[28:29], v22 offset:45056
	ds_read_b64_tr_b16 v[30:31], v22 offset:45568
	ds_read_b64_tr_b16 v[40:41], v23 offset:40960
	ds_read_b64_tr_b16 v[42:43], v23 offset:41472
	ds_read_b64_tr_b16 v[20:21], v23 offset:45056
	ds_read_b64_tr_b16 v[22:23], v23 offset:45568
	s_add_i32 s17, s16, s29
	v_add_u32_e32 v66, s17, v138
	v_add_u32_e32 v67, v66, v148
	v_add_u32_e32 v68, s50, v149
	ds_read_b128 v[74:77], v67
	ds_read_b128 v[78:81], v68
	v_add_u32_e32 v67, s51, v149
	v_add_u32_e32 v68, v66, v150
	ds_read_b128 v[90:93], v67
	ds_read_b128 v[82:85], v68
	v_add_u32_e32 v67, s50, v151
	v_add_u32_e32 v68, s51, v151
	ds_read_b128 v[98:101], v67
	ds_read_b128 v[102:105], v68
	v_add_u32_e32 v67, v66, v152
	v_add_u32_e32 v68, s50, v153
	ds_read_b128 v[86:89], v67
	ds_read_b128 v[110:113], v68
	v_add_u32_e32 v67, s51, v153
	v_add_u32_e32 v66, v66, v154
	v_add_u32_e32 v70, s50, v155
	v_add_u32_e32 v71, s51, v155
	v_add_u32_e32 v116, s16, v139
	ds_read_b128 v[106:109], v67
	ds_read_b128 v[66:69], v66
	ds_read_b128 v[94:97], v70
	ds_read_b128 v[70:73], v71
	ds_read_b128 v[116:119], v116 offset:49152
	s_and_b64 s[68:69], s[14:15], exec
	v_readlane_b32 s11, v254, 48
	s_cselect_b32 s18, s11, 0
	s_add_i32 s70, s60, s62
	s_ashr_i32 s71, s70, 31
	s_lshl_b64 s[72:73], s[70:71], 14
	s_add_u32 s74, s52, s72
	s_addc_u32 s75, s53, s73
	s_add_u32 s76, s74, 0x400
	s_addc_u32 s77, s75, 0
	s_add_u32 s78, s54, s72
	s_addc_u32 s79, s55, s73
	s_add_u32 s80, s78, 0x400
	s_addc_u32 s81, s79, 0
	s_lshl_b64 s[72:73], s[70:71], 13
	s_add_u32 s82, s35, s72
	s_addc_u32 s83, s36, s73
	s_lshl_b64 s[72:73], s[70:71], 9
	s_add_u32 s84, s40, s72
	s_addc_u32 s85, s41, s73
	s_add_i32 s86, s18, s24
	s_add_i32 s87, s18, s26
	s_add_i32 s88, s86, 0x4000
	s_add_i32 s89, s87, 0x4000
	s_add_i32 s90, s48, s18
	s_add_i32 s91, s49, s18
	s_add_i32 s92, s18, 0xc000
	s_add_i32 s93, s62, -4
	s_sub_i32 s94, s61, 64
	s_and_b64 s[68:69], s[12:13], exec
	s_cselect_b32 s93, s93, s61
	s_cselect_b32 s94, s62, s94
	s_lshl_b32 s93, s93, 6
	s_lshl_b32 s94, s94, 6
	s_or_b32 s94, s94, 0x1000
	s_cmp_gt_u32 s63, 1
	s_cselect_b32 s93, s93, s94
	s_add_i32 s93, s93, s57
	s_mul_hi_i32 s95, s93, 0x1800
	s_mul_i32 s94, s93, 0x1800
	s_add_u32 s94, s58, s94
	s_addc_u32 s95, s59, s95
	s_add_u32 s94, s94, 0x800
	s_addc_u32 s95, s95, 0
	s_waitcnt lgkmcnt(0)
	s_cmpk_gt_u32 s63, 0x41
	s_waitcnt lgkmcnt(0)
	s_barrier
	s_cbranch_scc1 .LBB0_490
	s_mov_b32 m0, s86
	s_nop 0
	global_load_lds_dwordx4 v65, s[74:75]
	s_mov_b32 m0, s87
	s_nop 0
	global_load_lds_dwordx4 v65, s[76:77]
	s_mov_b32 m0, s88
	s_nop 0
	global_load_lds_dwordx4 v65, s[78:79]
	s_mov_b32 m0, s89
	s_nop 0
	global_load_lds_dwordx4 v65, s[80:81]
	s_mov_b32 m0, s90
	s_nop 0
	global_load_lds_dwordx4 v65, s[82:83]
	s_mov_b32 m0, s91
	s_nop 0
	global_load_lds_dwordx4 v114, s[94:95]
	s_and_saveexec_b64 s[16:17], s[4:5]
	s_cbranch_execz .Lscan_cl_skip
	s_mov_b32 m0, s92
	s_nop 0
	global_load_lds_dwordx4 v65, s[84:85]

.LBB0_490:
	s_andn2_b64 vcc, exec, s[6:7]
	s_cbranch_vccnz .LBB0_510
	v_mfma_f32_16x16x32_bf16 v[120:123], v[44:47], v[56:59], 0
	v_mfma_f32_16x16x32_bf16 v[124:127], v[40:43], v[56:59], 0
	v_mfma_f32_16x16x32_bf16 v[120:123], v[28:31], v[60:63], v[120:123]
	v_mfma_f32_16x16x32_bf16 v[124:127], v[20:23], v[60:63], v[124:127]
	s_cbranch_execnz .LBB0_472
	s_branch .LBB0_511
.LBB0_510:
.LBB0_511:
	v_mfma_f32_16x16x32_bf16 v[120:123], v[52:55], v[56:59], 0
	v_mfma_f32_16x16x32_bf16 v[56:59], v[48:51], v[56:59], 0
	v_mfma_f32_16x16x32_bf16 v[120:123], v[36:39], v[60:63], v[120:123]
	v_mfma_f32_16x16x32_bf16 v[124:127], v[32:35], v[60:63], v[56:59]
	s_branch .LBB0_472
